# v6 + nt policy on the expert GEMM epilogue stores (act, yb)
# baseline (speedup 1.0000x reference)
.LBB0_1284:
	s_ashr_i32 s30, s28, 4
	s_lshl_b32 s25, s28, 7
	s_ashr_i32 s31, s30, 31
	s_and_b32 s25, s25, 0x780
	s_lshl_b64 s[30:31], s[30:31], 14
	v_or_b32_e32 v20, s25, v224
	s_add_u32 s30, s16, s30
	s_addc_u32 s31, s17, s31
	v_lshlrev_b32_e32 v2, 3, v20
	v_mov_b32_e32 v3, v201
	s_nop 15
	s_nop 15
	v_lshl_add_u64 v[2:3], s[30:31], 0, v[2:3]
	flat_load_dwordx4 v[4:7], v[2:3] offset:16
	flat_load_dwordx4 v[14:17], v[2:3]
	flat_load_dwordx4 v[24:27], v[2:3] offset:48
	flat_load_dwordx4 v[28:31], v[2:3] offset:32
	v_mov_b32_e32 v32, v201
	v_mov_b32_e32 v33, v201
	v_lshl_add_u32 v22, s63, 8, v222
	v_ashrrev_i32_e32 v23, 31, v22
	v_lshlrev_b64 v[2:3], 11, v[22:23]
	v_mov_b32_e32 v21, v201
	v_lshl_add_u64 v[2:3], s[6:7], 0, v[2:3]
	v_lshl_add_u64 v[2:3], v[2:3], 0, v[20:21]
	v_or_b32_e32 v34, 16, v22
	v_ashrrev_i32_e32 v35, 31, v34
	s_waitcnt vmcnt(0) lgkmcnt(0)
	v_mov_b32_e32 v12, v4
	v_mov_b32_e32 v18, v14
	v_mov_b32_e32 v19, v16
	v_mov_b32_e32 v10, v28
	v_mov_b32_e32 v11, v30
	v_mov_b32_e32 v30, v29
	v_pk_fma_f32 v[28:29], v[190:191], s[0:1], v[18:19] op_sel_hi:[1,0,1]
	v_mov_b32_e32 v13, v6
	v_min_f32_e32 v28, 0x40e00000, v28
	v_min_f32_e32 v29, 0x40e00000, v29
	v_pk_mul_f32 v[46:47], v[28:29], s[20:21] op_sel_hi:[1,0]
	v_mov_b32_e32 v6, v5
	v_pk_mul_f32 v[46:47], v[46:47], s[22:23] op_sel_hi:[1,0]
	v_mov_b32_e32 v4, v24
	v_mov_b32_e32 v5, v26
	v_mov_b32_e32 v26, v25
	v_pk_fma_f32 v[24:25], v[192:193], s[0:1], v[12:13] op_sel_hi:[1,0,1]
	v_pk_fma_f32 v[38:39], v[186:187], s[0:1], v[10:11] op_sel_hi:[1,0,1]
	v_exp_f32_e32 v46, v46
	v_exp_f32_e32 v47, v47
	v_min_f32_e32 v24, 0x40e00000, v24
	v_min_f32_e32 v25, 0x40e00000, v25
	v_min_f32_e32 v38, 0x40e00000, v38
	v_min_f32_e32 v39, 0x40e00000, v39
	v_pk_mul_f32 v[48:49], v[24:25], s[20:21] op_sel_hi:[1,0]
	v_pk_mul_f32 v[50:51], v[38:39], s[20:21] op_sel_hi:[1,0]
	v_pk_mul_f32 v[48:49], v[48:49], s[22:23] op_sel_hi:[1,0]
	v_pk_mul_f32 v[50:51], v[50:51], s[22:23] op_sel_hi:[1,0]
	v_pk_fma_f32 v[36:37], v[188:189], s[0:1], v[4:5] op_sel_hi:[1,0,1]
	v_exp_f32_e32 v48, v48
	v_exp_f32_e32 v49, v49
	v_exp_f32_e32 v50, v50
	v_exp_f32_e32 v51, v51
	v_pk_add_f32 v[46:47], v[46:47], 1.0 op_sel_hi:[1,0]
	v_min_f32_e32 v36, 0x40e00000, v36
	v_min_f32_e32 v37, 0x40e00000, v37
	v_rcp_f32_e32 v46, v46
	v_rcp_f32_e32 v47, v47
	v_mov_b32_e32 v16, v15
	v_pk_mul_f32 v[52:53], v[36:37], s[20:21] op_sel_hi:[1,0]
	v_pk_add_f32 v[14:15], v[16:17], 1.0 op_sel_hi:[1,0]
	v_pk_mul_f32 v[52:53], v[52:53], s[22:23] op_sel_hi:[1,0]
	v_pk_fma_f32 v[40:41], v[182:183], s[0:1], v[14:15] op_sel_hi:[1,0,1]
	v_exp_f32_e32 v52, v52
	v_exp_f32_e32 v53, v53
	v_pk_add_f32 v[48:49], v[48:49], 1.0 op_sel_hi:[1,0]
	v_pk_add_f32 v[50:51], v[50:51], 1.0 op_sel_hi:[1,0]
	v_med3_f32 v40, v40, s1, v227
	v_med3_f32 v41, v41, s1, v227
	v_rcp_f32_e32 v48, v48
	v_rcp_f32_e32 v49, v49
	v_rcp_f32_e32 v50, v50
	v_rcp_f32_e32 v51, v51
	v_pk_mul_f32 v[28:29], v[28:29], v[46:47]
	v_pk_add_f32 v[16:17], v[6:7], 1.0 op_sel_hi:[1,0]
	v_pk_mul_f32 v[28:29], v[40:41], v[28:29]
	v_pk_add_f32 v[6:7], v[30:31], 1.0 op_sel_hi:[1,0]
	v_cvt_pk_fp8_f32 v32, v28, v29
	v_pk_fma_f32 v[30:31], v[184:185], s[0:1], v[16:17] op_sel_hi:[1,0,1]
	v_pk_fma_f32 v[44:45], v[178:179], s[0:1], v[6:7] op_sel_hi:[1,0,1]
	v_pk_add_f32 v[52:53], v[52:53], 1.0 op_sel_hi:[1,0]
	v_med3_f32 v30, v30, s1, v227
	v_med3_f32 v31, v31, s1, v227
	v_med3_f32 v44, v44, s1, v227
	v_med3_f32 v45, v45, s1, v227
	v_rcp_f32_e32 v52, v52
	v_rcp_f32_e32 v53, v53
	v_pk_mul_f32 v[24:25], v[24:25], v[48:49]
	v_pk_mul_f32 v[38:39], v[38:39], v[50:51]
	v_pk_add_f32 v[8:9], v[26:27], 1.0 op_sel_hi:[1,0]
	v_pk_fma_f32 v[26:27], v[174:175], s[0:1], v[18:19] op_sel_hi:[1,0,1]
	v_pk_mul_f32 v[38:39], v[44:45], v[38:39]
	v_pk_mul_f32 v[24:25], v[30:31], v[24:25]
	v_cvt_pk_fp8_f32 v33, v38, v39
	v_cvt_pk_fp8_f32 v32, v24, v25 op_sel:[0,0,1]
	v_min_f32_e32 v24, 0x40e00000, v26
	v_min_f32_e32 v25, 0x40e00000, v27
	v_pk_fma_f32 v[42:43], v[180:181], s[0:1], v[8:9] op_sel_hi:[1,0,1]
	v_pk_mul_f32 v[26:27], v[24:25], s[20:21] op_sel_hi:[1,0]
	v_med3_f32 v42, v42, s1, v227
	v_med3_f32 v43, v43, s1, v227
	v_pk_mul_f32 v[36:37], v[36:37], v[52:53]
	v_pk_mul_f32 v[26:27], v[26:27], s[22:23] op_sel_hi:[1,0]
	v_pk_mul_f32 v[28:29], v[42:43], v[36:37]
	v_exp_f32_e32 v26, v26
	v_exp_f32_e32 v27, v27
	v_cvt_pk_fp8_f32 v33, v28, v29 op_sel:[0,0,1]
	v_pk_fma_f32 v[28:29], v[176:177], s[0:1], v[12:13] op_sel_hi:[1,0,1]
	v_pk_fma_f32 v[30:31], v[172:173], s[0:1], v[16:17] op_sel_hi:[1,0,1]
	v_min_f32_e32 v28, 0x40e00000, v28
	v_min_f32_e32 v29, 0x40e00000, v29
	v_pk_mul_f32 v[36:37], v[28:29], s[20:21] op_sel_hi:[1,0]
	v_pk_add_f32 v[26:27], v[26:27], 1.0 op_sel_hi:[1,0]
	v_pk_mul_f32 v[36:37], v[36:37], s[22:23] op_sel_hi:[1,0]
	v_rcp_f32_e32 v26, v26
	v_rcp_f32_e32 v27, v27
	v_exp_f32_e32 v36, v36
	v_exp_f32_e32 v37, v37
	global_store_dwordx2 v[2:3], v[32:33], off nt
	v_pk_mul_f32 v[24:25], v[24:25], v[26:27]
	v_pk_fma_f32 v[32:33], v[170:171], s[0:1], v[14:15] op_sel_hi:[1,0,1]
	v_pk_add_f32 v[26:27], v[36:37], 1.0 op_sel_hi:[1,0]
	v_med3_f32 v32, v32, s1, v227
	v_rcp_f32_e32 v26, v26
	v_rcp_f32_e32 v27, v27
	v_med3_f32 v33, v33, s1, v227
	v_pk_mul_f32 v[24:25], v[32:33], v[24:25]
	v_med3_f32 v30, v30, s1, v227
	v_pk_mul_f32 v[26:27], v[28:29], v[26:27]
	v_pk_fma_f32 v[28:29], v[166:167], s[0:1], v[10:11] op_sel_hi:[1,0,1]
	v_med3_f32 v31, v31, s1, v227
	v_min_f32_e32 v28, 0x40e00000, v28
	v_min_f32_e32 v29, 0x40e00000, v29
	v_pk_mul_f32 v[32:33], v[28:29], s[20:21] op_sel_hi:[1,0]
	v_pk_mul_f32 v[26:27], v[30:31], v[26:27]
	v_pk_mul_f32 v[32:33], v[32:33], s[22:23] op_sel_hi:[1,0]
	v_pk_fma_f32 v[30:31], v[168:169], s[0:1], v[4:5] op_sel_hi:[1,0,1]
	v_exp_f32_e32 v32, v32
	v_exp_f32_e32 v33, v33
	v_pk_fma_f32 v[38:39], v[162:163], s[0:1], v[6:7] op_sel_hi:[1,0,1]
	v_min_f32_e32 v30, 0x40e00000, v30
	v_min_f32_e32 v31, 0x40e00000, v31
	v_pk_add_f32 v[32:33], v[32:33], 1.0 op_sel_hi:[1,0]
	v_med3_f32 v38, v38, s1, v227
	v_rcp_f32_e32 v32, v32
	v_rcp_f32_e32 v33, v33
	v_med3_f32 v39, v39, s1, v227
	v_pk_fma_f32 v[36:37], v[164:165], s[0:1], v[8:9] op_sel_hi:[1,0,1]
	v_pk_mul_f32 v[28:29], v[28:29], v[32:33]
	v_pk_mul_f32 v[32:33], v[30:31], s[20:21] op_sel_hi:[1,0]
	v_pk_mul_f32 v[28:29], v[38:39], v[28:29]
	v_pk_mul_f32 v[32:33], v[32:33], s[22:23] op_sel_hi:[1,0]
	v_mov_b32_e32 v38, v201
	v_exp_f32_e32 v32, v32
	v_exp_f32_e32 v33, v33
	v_cvt_pk_fp8_f32 v38, v24, v25
	v_mov_b32_e32 v39, v201
	v_cvt_pk_fp8_f32 v39, v28, v29
	v_pk_add_f32 v[32:33], v[32:33], 1.0 op_sel_hi:[1,0]
	v_cvt_pk_fp8_f32 v38, v26, v27 op_sel:[0,0,1]
	v_pk_fma_f32 v[26:27], v[158:159], s[0:1], v[18:19] op_sel_hi:[1,0,1]
	v_rcp_f32_e32 v32, v32
	v_rcp_f32_e32 v33, v33
	v_min_f32_e32 v26, 0x40e00000, v26
	v_min_f32_e32 v27, 0x40e00000, v27
	v_pk_mul_f32 v[28:29], v[26:27], s[20:21] op_sel_hi:[1,0]
	v_pk_mul_f32 v[24:25], v[30:31], v[32:33]
	v_pk_mul_f32 v[28:29], v[28:29], s[22:23] op_sel_hi:[1,0]
	v_pk_fma_f32 v[30:31], v[160:161], s[0:1], v[12:13] op_sel_hi:[1,0,1]
	v_exp_f32_e32 v28, v28
	v_exp_f32_e32 v29, v29
	v_med3_f32 v36, v36, s1, v227
	v_med3_f32 v37, v37, s1, v227
	v_min_f32_e32 v30, 0x40e00000, v30
	v_min_f32_e32 v31, 0x40e00000, v31
	v_pk_mul_f32 v[24:25], v[36:37], v[24:25]
	v_pk_mul_f32 v[36:37], v[30:31], s[20:21] op_sel_hi:[1,0]
	v_pk_add_f32 v[28:29], v[28:29], 1.0 op_sel_hi:[1,0]
	v_pk_mul_f32 v[36:37], v[36:37], s[22:23] op_sel_hi:[1,0]
	v_rcp_f32_e32 v28, v28
	v_rcp_f32_e32 v29, v29
	v_exp_f32_e32 v36, v36
	v_exp_f32_e32 v37, v37
	v_cvt_pk_fp8_f32 v39, v24, v25 op_sel:[0,0,1]
	v_pk_mul_f32 v[26:27], v[26:27], v[28:29]
	v_lshlrev_b64 v[24:25], 11, v[34:35]
	v_pk_add_f32 v[28:29], v[36:37], 1.0 op_sel_hi:[1,0]
	v_pk_fma_f32 v[34:35], v[154:155], s[0:1], v[14:15] op_sel_hi:[1,0,1]
	v_rcp_f32_e32 v28, v28
	v_rcp_f32_e32 v29, v29
	v_med3_f32 v34, v34, s1, v227
	v_med3_f32 v35, v35, s1, v227
	v_pk_mul_f32 v[26:27], v[34:35], v[26:27]
	v_pk_mul_f32 v[28:29], v[30:31], v[28:29]
	v_pk_fma_f32 v[30:31], v[150:151], s[0:1], v[10:11] op_sel_hi:[1,0,1]
	v_pk_fma_f32 v[32:33], v[156:157], s[0:1], v[16:17] op_sel_hi:[1,0,1]
	v_min_f32_e32 v30, 0x40e00000, v30
	v_min_f32_e32 v31, 0x40e00000, v31
	v_pk_mul_f32 v[34:35], v[30:31], s[20:21] op_sel_hi:[1,0]
	v_med3_f32 v32, v32, s1, v227
	v_pk_mul_f32 v[34:35], v[34:35], s[22:23] op_sel_hi:[1,0]
	v_med3_f32 v33, v33, s1, v227
	v_exp_f32_e32 v34, v34
	v_exp_f32_e32 v35, v35
	v_pk_mul_f32 v[28:29], v[32:33], v[28:29]
	v_pk_fma_f32 v[32:33], v[152:153], s[0:1], v[4:5] op_sel_hi:[1,0,1]
	v_lshl_add_u64 v[24:25], s[6:7], 0, v[24:25]
	v_pk_add_f32 v[34:35], v[34:35], 1.0 op_sel_hi:[1,0]
	v_min_f32_e32 v32, 0x40e00000, v32
	v_rcp_f32_e32 v34, v34
	v_rcp_f32_e32 v35, v35
	v_min_f32_e32 v33, 0x40e00000, v33
	v_lshl_add_u64 v[24:25], v[24:25], 0, v[20:21]
	global_store_dwordx2 v[24:25], v[38:39], off nt
	v_pk_mul_f32 v[30:31], v[30:31], v[34:35]
	v_pk_mul_f32 v[34:35], v[32:33], s[20:21] op_sel_hi:[1,0]
	v_pk_fma_f32 v[38:39], v[146:147], s[0:1], v[6:7] op_sel_hi:[1,0,1]
	v_pk_mul_f32 v[34:35], v[34:35], s[22:23] op_sel_hi:[1,0]
	v_med3_f32 v38, v38, s1, v227
	v_exp_f32_e32 v34, v34
	v_exp_f32_e32 v35, v35
	v_med3_f32 v39, v39, s1, v227
	v_pk_mul_f32 v[30:31], v[38:39], v[30:31]
	v_mov_b32_e32 v38, v201
	v_pk_add_f32 v[34:35], v[34:35], 1.0 op_sel_hi:[1,0]
	v_mov_b32_e32 v39, v201
	v_rcp_f32_e32 v34, v34
	v_rcp_f32_e32 v35, v35
	v_cvt_pk_fp8_f32 v38, v26, v27
	v_cvt_pk_fp8_f32 v39, v30, v31
	v_pk_fma_f32 v[36:37], v[148:149], s[0:1], v[8:9] op_sel_hi:[1,0,1]
	v_pk_mul_f32 v[26:27], v[32:33], v[34:35]
	v_med3_f32 v36, v36, s1, v227
	v_med3_f32 v37, v37, s1, v227
	v_or_b32_e32 v24, 32, v22
	v_pk_mul_f32 v[26:27], v[36:37], v[26:27]
	v_ashrrev_i32_e32 v25, 31, v24
	v_cvt_pk_fp8_f32 v38, v28, v29 op_sel:[0,0,1]
	v_cvt_pk_fp8_f32 v39, v26, v27 op_sel:[0,0,1]
	v_lshlrev_b64 v[24:25], 11, v[24:25]
	v_lshl_add_u64 v[24:25], s[6:7], 0, v[24:25]
	v_lshl_add_u64 v[24:25], v[24:25], 0, v[20:21]
	global_store_dwordx2 v[24:25], v[38:39], off nt
	v_pk_fma_f32 v[24:25], v[142:143], s[0:1], v[18:19] op_sel_hi:[1,0,1]
	v_pk_fma_f32 v[28:29], v[144:145], s[0:1], v[12:13] op_sel_hi:[1,0,1]
	v_min_f32_e32 v24, 0x40e00000, v24
	v_min_f32_e32 v25, 0x40e00000, v25
	v_pk_mul_f32 v[26:27], v[24:25], s[20:21] op_sel_hi:[1,0]
	v_min_f32_e32 v28, 0x40e00000, v28
	v_pk_mul_f32 v[26:27], v[26:27], s[22:23] op_sel_hi:[1,0]
	v_min_f32_e32 v29, 0x40e00000, v29
	v_exp_f32_e32 v26, v26
	v_exp_f32_e32 v27, v27
	v_pk_mul_f32 v[34:35], v[28:29], s[20:21] op_sel_hi:[1,0]
	v_pk_fma_f32 v[32:33], v[138:139], s[0:1], v[14:15] op_sel_hi:[1,0,1]
	v_pk_mul_f32 v[34:35], v[34:35], s[22:23] op_sel_hi:[1,0]
	v_pk_add_f32 v[26:27], v[26:27], 1.0 op_sel_hi:[1,0]
	v_exp_f32_e32 v34, v34
	v_rcp_f32_e32 v26, v26
	v_rcp_f32_e32 v27, v27
	v_exp_f32_e32 v35, v35
	v_med3_f32 v32, v32, s1, v227
	v_med3_f32 v33, v33, s1, v227
	v_pk_mul_f32 v[24:25], v[24:25], v[26:27]
	v_pk_add_f32 v[26:27], v[34:35], 1.0 op_sel_hi:[1,0]
	v_pk_mul_f32 v[24:25], v[32:33], v[24:25]
	v_rcp_f32_e32 v26, v26
	v_rcp_f32_e32 v27, v27
	v_pk_fma_f32 v[30:31], v[140:141], s[0:1], v[16:17] op_sel_hi:[1,0,1]
	v_pk_fma_f32 v[36:37], v[130:131], s[0:1], v[6:7] op_sel_hi:[1,0,1]
	v_med3_f32 v30, v30, s1, v227
	v_pk_mul_f32 v[26:27], v[28:29], v[26:27]
	v_pk_fma_f32 v[28:29], v[134:135], s[0:1], v[10:11] op_sel_hi:[1,0,1]
	v_med3_f32 v31, v31, s1, v227
	v_min_f32_e32 v28, 0x40e00000, v28
	v_min_f32_e32 v29, 0x40e00000, v29
	v_pk_mul_f32 v[32:33], v[28:29], s[20:21] op_sel_hi:[1,0]
	v_pk_mul_f32 v[26:27], v[30:31], v[26:27]
	v_pk_mul_f32 v[32:33], v[32:33], s[22:23] op_sel_hi:[1,0]
	v_pk_fma_f32 v[30:31], v[136:137], s[0:1], v[4:5] op_sel_hi:[1,0,1]
	v_exp_f32_e32 v32, v32
	v_exp_f32_e32 v33, v33
	v_min_f32_e32 v30, 0x40e00000, v30
	v_min_f32_e32 v31, 0x40e00000, v31
	v_med3_f32 v36, v36, s1, v227
	v_pk_add_f32 v[32:33], v[32:33], 1.0 op_sel_hi:[1,0]
	v_med3_f32 v37, v37, s1, v227
	v_rcp_f32_e32 v32, v32
	v_rcp_f32_e32 v33, v33
	v_pk_fma_f32 v[34:35], v[132:133], s[0:1], v[8:9] op_sel_hi:[1,0,1]
	v_or_b32_e32 v22, 48, v22
	v_med3_f32 v34, v34, s1, v227
	v_pk_mul_f32 v[28:29], v[28:29], v[32:33]
	v_pk_mul_f32 v[32:33], v[30:31], s[20:21] op_sel_hi:[1,0]
	v_pk_mul_f32 v[28:29], v[36:37], v[28:29]
	v_pk_mul_f32 v[32:33], v[32:33], s[22:23] op_sel_hi:[1,0]
	v_mov_b32_e32 v36, v201
	v_exp_f32_e32 v32, v32
	v_exp_f32_e32 v33, v33
	v_mov_b32_e32 v37, v201
	v_cvt_pk_fp8_f32 v36, v24, v25
	v_cvt_pk_fp8_f32 v37, v28, v29
	v_pk_add_f32 v[32:33], v[32:33], 1.0 op_sel_hi:[1,0]
	v_med3_f32 v35, v35, s1, v227
	v_rcp_f32_e32 v32, v32
	v_rcp_f32_e32 v33, v33
	v_ashrrev_i32_e32 v23, 31, v22
	v_cvt_pk_fp8_f32 v36, v26, v27 op_sel:[0,0,1]
	v_lshlrev_b64 v[22:23], 11, v[22:23]
	v_pk_mul_f32 v[24:25], v[30:31], v[32:33]
	v_lshl_add_u64 v[22:23], s[6:7], 0, v[22:23]
	v_pk_mul_f32 v[24:25], v[34:35], v[24:25]
	v_lshl_add_u64 v[20:21], v[22:23], 0, v[20:21]
	v_cvt_pk_fp8_f32 v37, v24, v25 op_sel:[0,0,1]
	v_pk_fma_f32 v[24:25], v[128:129], s[0:1], v[12:13] op_sel_hi:[1,0,1]
	v_pk_fma_f32 v[28:29], v[122:123], s[0:1], v[14:15] op_sel_hi:[1,0,1]
	v_min_f32_e32 v24, 0x40e00000, v24
	global_store_dwordx2 v[20:21], v[36:37], off nt
	v_pk_fma_f32 v[20:21], v[126:127], s[0:1], v[18:19] op_sel_hi:[1,0,1]
	v_min_f32_e32 v25, 0x40e00000, v25
	v_min_f32_e32 v20, 0x40e00000, v20
	v_min_f32_e32 v21, 0x40e00000, v21
	v_pk_mul_f32 v[22:23], v[20:21], s[20:21] op_sel_hi:[1,0]
	v_pk_mul_f32 v[30:31], v[24:25], s[20:21] op_sel_hi:[1,0]
	v_pk_mul_f32 v[22:23], v[22:23], s[22:23] op_sel_hi:[1,0]
	v_pk_mul_f32 v[30:31], v[30:31], s[22:23] op_sel_hi:[1,0]
	v_exp_f32_e32 v22, v22
	v_exp_f32_e32 v23, v23
	v_exp_f32_e32 v30, v30
	v_exp_f32_e32 v31, v31
	v_med3_f32 v28, v28, s1, v227
	v_pk_add_f32 v[22:23], v[22:23], 1.0 op_sel_hi:[1,0]
	v_med3_f32 v29, v29, s1, v227
	v_rcp_f32_e32 v22, v22
	v_rcp_f32_e32 v23, v23
	v_pk_fma_f32 v[26:27], v[124:125], s[0:1], v[16:17] op_sel_hi:[1,0,1]
	v_pk_fma_f32 v[32:33], v[114:115], s[0:1], v[6:7] op_sel_hi:[1,0,1]
	v_med3_f32 v26, v26, s1, v227
	v_pk_mul_f32 v[20:21], v[20:21], v[22:23]
	v_pk_add_f32 v[22:23], v[30:31], 1.0 op_sel_hi:[1,0]
	v_pk_mul_f32 v[20:21], v[28:29], v[20:21]
	v_rcp_f32_e32 v22, v22
	v_rcp_f32_e32 v23, v23
	v_med3_f32 v27, v27, s1, v227
	v_med3_f32 v32, v32, s1, v227
	v_med3_f32 v33, v33, s1, v227
	v_pk_mul_f32 v[22:23], v[24:25], v[22:23]
	v_pk_fma_f32 v[24:25], v[118:119], s[0:1], v[10:11] op_sel_hi:[1,0,1]
	v_pk_mul_f32 v[22:23], v[26:27], v[22:23]
	v_min_f32_e32 v24, 0x40e00000, v24
	v_min_f32_e32 v25, 0x40e00000, v25
	v_pk_mul_f32 v[28:29], v[24:25], s[20:21] op_sel_hi:[1,0]
	v_pk_fma_f32 v[26:27], v[120:121], s[0:1], v[4:5] op_sel_hi:[1,0,1]
	v_pk_mul_f32 v[28:29], v[28:29], s[22:23] op_sel_hi:[1,0]
	v_min_f32_e32 v26, 0x40e00000, v26
	v_exp_f32_e32 v28, v28
	v_exp_f32_e32 v29, v29
	v_min_f32_e32 v27, 0x40e00000, v27
	v_pk_fma_f32 v[30:31], v[116:117], s[0:1], v[8:9] op_sel_hi:[1,0,1]
	v_pk_add_f32 v[28:29], v[28:29], 1.0 op_sel_hi:[1,0]
	s_nop 0
	v_rcp_f32_e32 v28, v28
	v_rcp_f32_e32 v29, v29
	v_med3_f32 v30, v30, s1, v227
	v_med3_f32 v31, v31, s1, v227
	v_pk_mul_f32 v[24:25], v[24:25], v[28:29]
	v_pk_mul_f32 v[28:29], v[26:27], s[20:21] op_sel_hi:[1,0]
	v_pk_mul_f32 v[24:25], v[32:33], v[24:25]
	v_pk_mul_f32 v[28:29], v[28:29], s[22:23] op_sel_hi:[1,0]
	v_mov_b32_e32 v32, v201
	v_exp_f32_e32 v28, v28
	v_exp_f32_e32 v29, v29
	v_mov_b32_e32 v33, v201
	v_cvt_pk_fp8_f32 v32, v20, v21
	v_cvt_pk_fp8_f32 v33, v24, v25
	v_pk_add_f32 v[28:29], v[28:29], 1.0 op_sel_hi:[1,0]
	v_pk_fma_f32 v[24:25], v[112:113], s[0:1], v[12:13] op_sel_hi:[1,0,1]
	v_rcp_f32_e32 v28, v28
	v_rcp_f32_e32 v29, v29
	v_cvt_pk_fp8_f32 v32, v22, v23 op_sel:[0,0,1]
	v_min_f32_e32 v24, 0x40e00000, v24
	v_min_f32_e32 v25, 0x40e00000, v25
	v_pk_mul_f32 v[20:21], v[26:27], v[28:29]
	v_pk_fma_f32 v[28:29], v[106:107], s[0:1], v[14:15] op_sel_hi:[1,0,1]
	v_pk_mul_f32 v[20:21], v[30:31], v[20:21]
	v_pk_mul_f32 v[30:31], v[24:25], s[20:21] op_sel_hi:[1,0]
	v_cvt_pk_fp8_f32 v33, v20, v21 op_sel:[0,0,1]
	v_add_co_u32_e32 v20, vcc, s57, v2
	v_pk_mul_f32 v[30:31], v[30:31], s[22:23] op_sel_hi:[1,0]
	s_nop 0
	v_addc_co_u32_e32 v21, vcc, 0, v3, vcc
	global_store_dwordx2 v[20:21], v[32:33], off nt
	v_pk_fma_f32 v[20:21], v[110:111], s[0:1], v[18:19] op_sel_hi:[1,0,1]
	v_exp_f32_e32 v30, v30
	v_min_f32_e32 v20, 0x40e00000, v20
	v_min_f32_e32 v21, 0x40e00000, v21
	v_pk_mul_f32 v[22:23], v[20:21], s[20:21] op_sel_hi:[1,0]
	v_exp_f32_e32 v31, v31
	v_pk_mul_f32 v[22:23], v[22:23], s[22:23] op_sel_hi:[1,0]
	v_med3_f32 v28, v28, s1, v227
	v_exp_f32_e32 v22, v22
	v_exp_f32_e32 v23, v23
	v_med3_f32 v29, v29, s1, v227
	v_pk_fma_f32 v[26:27], v[108:109], s[0:1], v[16:17] op_sel_hi:[1,0,1]
	v_pk_fma_f32 v[32:33], v[98:99], s[0:1], v[6:7] op_sel_hi:[1,0,1]
	v_pk_add_f32 v[22:23], v[22:23], 1.0 op_sel_hi:[1,0]
	v_med3_f32 v26, v26, s1, v227
	v_rcp_f32_e32 v22, v22
	v_rcp_f32_e32 v23, v23
	v_med3_f32 v27, v27, s1, v227
	v_med3_f32 v32, v32, s1, v227
	v_med3_f32 v33, v33, s1, v227
	v_pk_mul_f32 v[20:21], v[20:21], v[22:23]
	v_pk_add_f32 v[22:23], v[30:31], 1.0 op_sel_hi:[1,0]
	v_pk_mul_f32 v[20:21], v[28:29], v[20:21]
	v_rcp_f32_e32 v22, v22
	v_rcp_f32_e32 v23, v23
	v_pk_fma_f32 v[30:31], v[100:101], s[0:1], v[8:9] op_sel_hi:[1,0,1]
	v_pk_mul_f32 v[22:23], v[24:25], v[22:23]
	v_pk_fma_f32 v[24:25], v[102:103], s[0:1], v[10:11] op_sel_hi:[1,0,1]
	v_pk_mul_f32 v[22:23], v[26:27], v[22:23]
	v_min_f32_e32 v24, 0x40e00000, v24
	v_min_f32_e32 v25, 0x40e00000, v25
	v_pk_mul_f32 v[28:29], v[24:25], s[20:21] op_sel_hi:[1,0]
	v_pk_fma_f32 v[26:27], v[104:105], s[0:1], v[4:5] op_sel_hi:[1,0,1]
	v_pk_mul_f32 v[28:29], v[28:29], s[22:23] op_sel_hi:[1,0]
	v_min_f32_e32 v26, 0x40e00000, v26
	v_exp_f32_e32 v28, v28
	v_exp_f32_e32 v29, v29
	v_min_f32_e32 v27, 0x40e00000, v27
	v_med3_f32 v30, v30, s1, v227
	v_med3_f32 v31, v31, s1, v227
	v_pk_add_f32 v[28:29], v[28:29], 1.0 op_sel_hi:[1,0]
	s_nop 0
	v_rcp_f32_e32 v28, v28
	v_rcp_f32_e32 v29, v29
	s_nop 0
	v_pk_mul_f32 v[24:25], v[24:25], v[28:29]
	v_pk_mul_f32 v[28:29], v[26:27], s[20:21] op_sel_hi:[1,0]
	v_pk_mul_f32 v[24:25], v[32:33], v[24:25]
	v_pk_mul_f32 v[28:29], v[28:29], s[22:23] op_sel_hi:[1,0]
	v_mov_b32_e32 v32, v201
	v_exp_f32_e32 v28, v28
	v_exp_f32_e32 v29, v29
	v_mov_b32_e32 v33, v201
	v_cvt_pk_fp8_f32 v32, v20, v21
	v_cvt_pk_fp8_f32 v33, v24, v25
	v_pk_add_f32 v[28:29], v[28:29], 1.0 op_sel_hi:[1,0]
	v_pk_fma_f32 v[24:25], v[96:97], s[0:1], v[12:13] op_sel_hi:[1,0,1]
	v_rcp_f32_e32 v28, v28
	v_rcp_f32_e32 v29, v29
	v_cvt_pk_fp8_f32 v32, v22, v23 op_sel:[0,0,1]
	v_min_f32_e32 v24, 0x40e00000, v24
	v_min_f32_e32 v25, 0x40e00000, v25
	v_pk_mul_f32 v[20:21], v[26:27], v[28:29]
	v_pk_fma_f32 v[28:29], v[90:91], s[0:1], v[14:15] op_sel_hi:[1,0,1]
	v_pk_mul_f32 v[20:21], v[30:31], v[20:21]
	v_pk_mul_f32 v[30:31], v[24:25], s[20:21] op_sel_hi:[1,0]
	v_cvt_pk_fp8_f32 v33, v20, v21 op_sel:[0,0,1]
	v_add_co_u32_e32 v20, vcc, s58, v2
	v_pk_mul_f32 v[30:31], v[30:31], s[22:23] op_sel_hi:[1,0]
	s_nop 0
	v_addc_co_u32_e32 v21, vcc, 0, v3, vcc
	global_store_dwordx2 v[20:21], v[32:33], off nt
	v_pk_fma_f32 v[20:21], v[94:95], s[0:1], v[18:19] op_sel_hi:[1,0,1]
	v_exp_f32_e32 v30, v30
	v_min_f32_e32 v20, 0x40e00000, v20
	v_min_f32_e32 v21, 0x40e00000, v21
	v_pk_mul_f32 v[22:23], v[20:21], s[20:21] op_sel_hi:[1,0]
	v_exp_f32_e32 v31, v31
	v_pk_mul_f32 v[22:23], v[22:23], s[22:23] op_sel_hi:[1,0]
	v_med3_f32 v28, v28, s1, v227
	v_exp_f32_e32 v22, v22
	v_exp_f32_e32 v23, v23
	v_med3_f32 v29, v29, s1, v227
	v_pk_fma_f32 v[26:27], v[92:93], s[0:1], v[16:17] op_sel_hi:[1,0,1]
	v_pk_fma_f32 v[32:33], v[82:83], s[0:1], v[6:7] op_sel_hi:[1,0,1]
	v_pk_add_f32 v[22:23], v[22:23], 1.0 op_sel_hi:[1,0]
	v_med3_f32 v26, v26, s1, v227
	v_rcp_f32_e32 v22, v22
	v_rcp_f32_e32 v23, v23
	v_med3_f32 v27, v27, s1, v227
	v_med3_f32 v32, v32, s1, v227
	v_med3_f32 v33, v33, s1, v227
	v_pk_mul_f32 v[20:21], v[20:21], v[22:23]
	v_pk_add_f32 v[22:23], v[30:31], 1.0 op_sel_hi:[1,0]
	v_pk_mul_f32 v[20:21], v[28:29], v[20:21]
	v_rcp_f32_e32 v22, v22
	v_rcp_f32_e32 v23, v23
	v_pk_fma_f32 v[30:31], v[84:85], s[0:1], v[8:9] op_sel_hi:[1,0,1]
	v_pk_fma_f32 v[18:19], v[78:79], s[0:1], v[18:19] op_sel_hi:[1,0,1]
	v_med3_f32 v30, v30, s1, v227
	v_pk_mul_f32 v[22:23], v[24:25], v[22:23]
	v_pk_fma_f32 v[24:25], v[86:87], s[0:1], v[10:11] op_sel_hi:[1,0,1]
	v_pk_mul_f32 v[22:23], v[26:27], v[22:23]
	v_min_f32_e32 v24, 0x40e00000, v24
	v_min_f32_e32 v25, 0x40e00000, v25
	v_pk_mul_f32 v[28:29], v[24:25], s[20:21] op_sel_hi:[1,0]
	v_pk_fma_f32 v[26:27], v[88:89], s[0:1], v[4:5] op_sel_hi:[1,0,1]
	v_pk_mul_f32 v[28:29], v[28:29], s[22:23] op_sel_hi:[1,0]
	v_min_f32_e32 v26, 0x40e00000, v26
	v_exp_f32_e32 v28, v28
	v_exp_f32_e32 v29, v29
	v_min_f32_e32 v27, 0x40e00000, v27
	v_med3_f32 v31, v31, s1, v227
	v_min_f32_e32 v18, 0x40e00000, v18
	v_pk_add_f32 v[28:29], v[28:29], 1.0 op_sel_hi:[1,0]
	v_min_f32_e32 v19, 0x40e00000, v19
	v_rcp_f32_e32 v28, v28
	v_rcp_f32_e32 v29, v29
	v_pk_fma_f32 v[12:13], v[80:81], s[0:1], v[12:13] op_sel_hi:[1,0,1]
	v_pk_fma_f32 v[14:15], v[74:75], s[0:1], v[14:15] op_sel_hi:[1,0,1]
	v_min_f32_e32 v12, 0x40e00000, v12
	v_pk_mul_f32 v[24:25], v[24:25], v[28:29]
	v_pk_mul_f32 v[28:29], v[26:27], s[20:21] op_sel_hi:[1,0]
	v_pk_mul_f32 v[24:25], v[32:33], v[24:25]
	v_pk_mul_f32 v[28:29], v[28:29], s[22:23] op_sel_hi:[1,0]
	v_mov_b32_e32 v32, v201
	v_exp_f32_e32 v28, v28
	v_exp_f32_e32 v29, v29
	v_mov_b32_e32 v33, v201
	v_cvt_pk_fp8_f32 v32, v20, v21
	v_cvt_pk_fp8_f32 v33, v24, v25
	v_pk_add_f32 v[28:29], v[28:29], 1.0 op_sel_hi:[1,0]
	v_min_f32_e32 v13, 0x40e00000, v13
	v_rcp_f32_e32 v28, v28
	v_rcp_f32_e32 v29, v29
	v_cvt_pk_fp8_f32 v32, v22, v23 op_sel:[0,0,1]
	v_pk_mul_f32 v[22:23], v[12:13], s[20:21] op_sel_hi:[1,0]
	v_pk_fma_f32 v[10:11], v[70:71], s[0:1], v[10:11] op_sel_hi:[1,0,1]
	v_pk_mul_f32 v[20:21], v[26:27], v[28:29]
	v_pk_mul_f32 v[22:23], v[22:23], s[22:23] op_sel_hi:[1,0]
	v_pk_mul_f32 v[20:21], v[30:31], v[20:21]
	v_exp_f32_e32 v22, v22
	v_cvt_pk_fp8_f32 v33, v20, v21 op_sel:[0,0,1]
	v_add_co_u32_e32 v20, vcc, s59, v2
	v_exp_f32_e32 v23, v23
	s_nop 0
	v_addc_co_u32_e32 v21, vcc, 0, v3, vcc
	global_store_dwordx2 v[20:21], v[32:33], off nt
	v_pk_mul_f32 v[20:21], v[18:19], s[20:21] op_sel_hi:[1,0]
	v_med3_f32 v14, v14, s1, v227
	v_pk_mul_f32 v[20:21], v[20:21], s[22:23] op_sel_hi:[1,0]
	v_med3_f32 v15, v15, s1, v227
	v_exp_f32_e32 v20, v20
	v_exp_f32_e32 v21, v21
	v_min_f32_e32 v10, 0x40e00000, v10
	v_min_f32_e32 v11, 0x40e00000, v11
	v_pk_fma_f32 v[16:17], v[76:77], s[0:1], v[16:17] op_sel_hi:[1,0,1]
	v_pk_add_f32 v[20:21], v[20:21], 1.0 op_sel_hi:[1,0]
	v_med3_f32 v16, v16, s1, v227
	v_rcp_f32_e32 v20, v20
	v_rcp_f32_e32 v21, v21
	v_med3_f32 v17, v17, s1, v227
	v_pk_fma_f32 v[4:5], v[72:73], s[0:1], v[4:5] op_sel_hi:[1,0,1]
	v_pk_fma_f32 v[6:7], v[66:67], s[0:1], v[6:7] op_sel_hi:[1,0,1]
	v_pk_mul_f32 v[18:19], v[18:19], v[20:21]
	v_pk_add_f32 v[20:21], v[22:23], 1.0 op_sel_hi:[1,0]
	v_pk_mul_f32 v[14:15], v[14:15], v[18:19]
	v_pk_mul_f32 v[18:19], v[10:11], s[20:21] op_sel_hi:[1,0]
	v_rcp_f32_e32 v20, v20
	v_rcp_f32_e32 v21, v21
	v_pk_mul_f32 v[18:19], v[18:19], s[22:23] op_sel_hi:[1,0]
	v_min_f32_e32 v4, 0x40e00000, v4
	v_exp_f32_e32 v18, v18
	v_exp_f32_e32 v19, v19
	v_pk_mul_f32 v[12:13], v[12:13], v[20:21]
	v_min_f32_e32 v5, 0x40e00000, v5
	v_pk_mul_f32 v[12:13], v[16:17], v[12:13]
	v_pk_add_f32 v[16:17], v[18:19], 1.0 op_sel_hi:[1,0]
	v_med3_f32 v6, v6, s1, v227
	v_rcp_f32_e32 v16, v16
	v_rcp_f32_e32 v17, v17
	v_med3_f32 v7, v7, s1, v227
	v_pk_fma_f32 v[8:9], v[68:69], s[0:1], v[8:9] op_sel_hi:[1,0,1]
	v_add_co_u32_e32 v2, vcc, 0x58000, v2
	v_pk_mul_f32 v[10:11], v[10:11], v[16:17]
	v_pk_mul_f32 v[16:17], v[4:5], s[20:21] op_sel_hi:[1,0]
	v_pk_mul_f32 v[6:7], v[6:7], v[10:11]
	v_pk_mul_f32 v[16:17], v[16:17], s[22:23] op_sel_hi:[1,0]
	v_med3_f32 v8, v8, s1, v227
	v_exp_f32_e32 v16, v16
	v_exp_f32_e32 v17, v17
	v_med3_f32 v9, v9, s1, v227
	v_addc_co_u32_e32 v3, vcc, 0, v3, vcc
	v_pk_add_f32 v[10:11], v[16:17], 1.0 op_sel_hi:[1,0]
	v_mov_b32_e32 v16, v201
	v_rcp_f32_e32 v10, v10
	v_rcp_f32_e32 v11, v11
	v_mov_b32_e32 v17, v201
	v_cvt_pk_fp8_f32 v16, v14, v15
	v_cvt_pk_fp8_f32 v17, v6, v7
	v_pk_mul_f32 v[4:5], v[4:5], v[10:11]
	s_andn2_b64 vcc, exec, s[8:9]
	v_pk_mul_f32 v[4:5], v[8:9], v[4:5]
	v_cvt_pk_fp8_f32 v16, v12, v13 op_sel:[0,0,1]
	v_cvt_pk_fp8_f32 v17, v4, v5 op_sel:[0,0,1]
	s_mov_b64 s[8:9], -1
	global_store_dwordx2 v[2:3], v[16:17], off nt
	s_cbranch_vccnz .LBB0_1267
	s_andn2_b64 vcc, exec, s[4:5]
	s_cbranch_vccnz .LBB0_1266
	s_barrier
	s_branch .LBB0_1266

.LBB0_1365:
	s_ashr_i32 s40, s38, 3
	s_lshl_b32 s27, s38, 8
	s_ashr_i32 s41, s40, 31
	s_and_b32 s27, s27, 0x700
	s_lshl_b64 s[40:41], s[40:41], 13
	v_or_b32_e32 v204, s27, v224
	s_add_u32 s40, s2, s40
	s_addc_u32 s41, s3, s41
	v_lshlrev_b32_e32 v2, 2, v204
	v_mov_b32_e32 v3, v205
	s_nop 15
	s_nop 15
	v_lshl_add_u64 v[2:3], s[40:41], 0, v[2:3]
	flat_load_dwordx4 v[14:17], v[2:3]
	flat_load_dwordx4 v[10:13], v[2:3] offset:16
	flat_load_dwordx4 v[6:9], v[2:3] offset:512
	s_nop 0
	flat_load_dwordx4 v[2:5], v[2:3] offset:528
	v_lshl_add_u32 v20, s36, 8, v1
	v_mbcnt_lo_u32_b32 v22, -1, 0
	v_ashrrev_i32_e32 v21, 31, v20
	v_mbcnt_hi_u32_b32 v22, -1, v22
	v_lshlrev_b64 v[20:21], 11, v[20:21]
	v_and_b32_e32 v22, 16, v22
	v_lshl_add_u64 v[20:21], s[10:11], 0, v[20:21]
	v_lshlrev_b32_e32 v23, 11, v22
	v_lshrrev_b32_e32 v22, 1, v22
	v_lshl_add_u64 v[18:19], v[20:21], 0, v[204:205]
	v_sub_u32_e32 v22, v23, v22
	v_mov_b32_e32 v23, v205
	v_mov_b32_e32 v24, 0x10000
	v_mov_b32_e32 v25, v205
	v_mov_b32_e32 v26, 0x40000
	v_mov_b32_e32 v27, v205
	v_lshl_add_u64 v[18:19], v[18:19], 0, v[22:23]
	s_waitcnt vmcnt(0) lgkmcnt(0)
	v_pk_fma_f32 v[28:29], v[190:191], s[16:17], v[14:15] op_sel_hi:[1,0,1]
	v_pk_fma_f32 v[30:31], v[192:193], s[16:17], v[16:17] op_sel_hi:[1,0,1]
	v_pk_fma_f32 v[32:33], v[186:187], s[16:17], v[10:11] op_sel_hi:[1,0,1]
	v_pk_fma_f32 v[34:35], v[188:189], s[16:17], v[12:13] op_sel_hi:[1,0,1]
	v_pk_fma_f32 v[36:37], v[182:183], s[16:17], v[14:15] op_sel_hi:[1,0,1]
	v_pk_fma_f32 v[38:39], v[184:185], s[16:17], v[16:17] op_sel_hi:[1,0,1]
	v_pk_fma_f32 v[40:41], v[178:179], s[16:17], v[10:11] op_sel_hi:[1,0,1]
	v_pk_fma_f32 v[42:43], v[180:181], s[16:17], v[12:13] op_sel_hi:[1,0,1]
	v_pk_mul_f32 v[28:29], v[28:29], s[18:19] op_sel_hi:[1,0]
	v_pk_mul_f32 v[30:31], v[30:31], s[18:19] op_sel_hi:[1,0]
	v_pk_mul_f32 v[32:33], v[32:33], s[18:19] op_sel_hi:[1,0]
	v_pk_mul_f32 v[34:35], v[34:35], s[18:19] op_sel_hi:[1,0]
	v_pk_mul_f32 v[36:37], v[36:37], s[18:19] op_sel_hi:[1,0]
	v_pk_mul_f32 v[38:39], v[38:39], s[18:19] op_sel_hi:[1,0]
	v_pk_mul_f32 v[40:41], v[40:41], s[18:19] op_sel_hi:[1,0]
	v_pk_mul_f32 v[42:43], v[42:43], s[18:19] op_sel_hi:[1,0]
	v_mov_b32_e32 v44, v205
	v_mov_b32_e32 v45, v205
	v_mov_b32_e32 v46, v205
	v_mov_b32_e32 v47, v205
	v_cvt_pk_fp8_f32 v44, v28, v29
	v_cvt_pk_fp8_f32 v45, v32, v33
	v_cvt_pk_fp8_f32 v46, v36, v37
	v_cvt_pk_fp8_f32 v47, v40, v41
	v_cvt_pk_fp8_f32 v44, v30, v31 op_sel:[0,0,1]
	v_cvt_pk_fp8_f32 v45, v34, v35 op_sel:[0,0,1]
	v_cvt_pk_fp8_f32 v46, v38, v39 op_sel:[0,0,1]
	v_cvt_pk_fp8_f32 v47, v42, v43 op_sel:[0,0,1]
	s_nop 1
	v_permlane16_swap_b32 v44, v46
	v_permlane16_swap_b32 v45, v47
	s_nop 1
	global_store_dwordx4 v[18:19], v[44:47], off nt
	v_pk_fma_f32 v[28:29], v[170:171], s[16:17], v[6:7] op_sel_hi:[1,0,1]
	v_pk_fma_f32 v[30:31], v[172:173], s[16:17], v[8:9] op_sel_hi:[1,0,1]
	v_pk_fma_f32 v[32:33], v[166:167], s[16:17], v[2:3] op_sel_hi:[1,0,1]
	v_pk_fma_f32 v[34:35], v[168:169], s[16:17], v[4:5] op_sel_hi:[1,0,1]
	v_pk_fma_f32 v[36:37], v[162:163], s[16:17], v[6:7] op_sel_hi:[1,0,1]
	v_pk_fma_f32 v[38:39], v[164:165], s[16:17], v[8:9] op_sel_hi:[1,0,1]
	v_pk_fma_f32 v[40:41], v[158:159], s[16:17], v[2:3] op_sel_hi:[1,0,1]
	v_pk_fma_f32 v[42:43], v[160:161], s[16:17], v[4:5] op_sel_hi:[1,0,1]
	v_pk_mul_f32 v[28:29], v[28:29], s[18:19] op_sel_hi:[1,0]
	v_pk_mul_f32 v[30:31], v[30:31], s[18:19] op_sel_hi:[1,0]
	v_pk_mul_f32 v[32:33], v[32:33], s[18:19] op_sel_hi:[1,0]
	v_pk_mul_f32 v[34:35], v[34:35], s[18:19] op_sel_hi:[1,0]
	v_pk_mul_f32 v[36:37], v[36:37], s[18:19] op_sel_hi:[1,0]
	v_pk_mul_f32 v[38:39], v[38:39], s[18:19] op_sel_hi:[1,0]
	v_pk_mul_f32 v[40:41], v[40:41], s[18:19] op_sel_hi:[1,0]
	v_pk_mul_f32 v[42:43], v[42:43], s[18:19] op_sel_hi:[1,0]
	v_mov_b32_e32 v48, v205
	v_mov_b32_e32 v49, v205
	v_mov_b32_e32 v50, v205
	v_mov_b32_e32 v51, v205
	v_cvt_pk_fp8_f32 v48, v28, v29
	v_cvt_pk_fp8_f32 v49, v32, v33
	v_cvt_pk_fp8_f32 v50, v36, v37
	v_cvt_pk_fp8_f32 v51, v40, v41
	v_cvt_pk_fp8_f32 v48, v30, v31 op_sel:[0,0,1]
	v_cvt_pk_fp8_f32 v49, v34, v35 op_sel:[0,0,1]
	v_cvt_pk_fp8_f32 v50, v38, v39 op_sel:[0,0,1]
	v_cvt_pk_fp8_f32 v51, v42, v43 op_sel:[0,0,1]
	s_nop 1
	v_permlane16_swap_b32 v48, v50
	v_permlane16_swap_b32 v49, v51
	s_nop 1
	global_store_dwordx4 v[18:19], v[48:51], off offset:128 nt
	v_lshl_add_u64 v[20:21], v[18:19], 0, v[24:25]
	v_pk_fma_f32 v[28:29], v[174:175], s[16:17], v[14:15] op_sel_hi:[1,0,1]
	v_pk_fma_f32 v[30:31], v[176:177], s[16:17], v[16:17] op_sel_hi:[1,0,1]
	v_pk_fma_f32 v[32:33], v[154:155], s[16:17], v[10:11] op_sel_hi:[1,0,1]
	v_pk_fma_f32 v[34:35], v[156:157], s[16:17], v[12:13] op_sel_hi:[1,0,1]
	v_pk_fma_f32 v[36:37], v[146:147], s[16:17], v[14:15] op_sel_hi:[1,0,1]
	v_pk_fma_f32 v[38:39], v[148:149], s[16:17], v[16:17] op_sel_hi:[1,0,1]
	v_pk_fma_f32 v[40:41], v[138:139], s[16:17], v[10:11] op_sel_hi:[1,0,1]
	v_pk_fma_f32 v[42:43], v[140:141], s[16:17], v[12:13] op_sel_hi:[1,0,1]
	v_pk_mul_f32 v[28:29], v[28:29], s[18:19] op_sel_hi:[1,0]
	v_pk_mul_f32 v[30:31], v[30:31], s[18:19] op_sel_hi:[1,0]
	v_pk_mul_f32 v[32:33], v[32:33], s[18:19] op_sel_hi:[1,0]
	v_pk_mul_f32 v[34:35], v[34:35], s[18:19] op_sel_hi:[1,0]
	v_pk_mul_f32 v[36:37], v[36:37], s[18:19] op_sel_hi:[1,0]
	v_pk_mul_f32 v[38:39], v[38:39], s[18:19] op_sel_hi:[1,0]
	v_pk_mul_f32 v[40:41], v[40:41], s[18:19] op_sel_hi:[1,0]
	v_pk_mul_f32 v[42:43], v[42:43], s[18:19] op_sel_hi:[1,0]
	v_mov_b32_e32 v44, v205
	v_mov_b32_e32 v45, v205
	v_mov_b32_e32 v46, v205
	v_mov_b32_e32 v47, v205
	v_cvt_pk_fp8_f32 v44, v28, v29
	v_cvt_pk_fp8_f32 v45, v32, v33
	v_cvt_pk_fp8_f32 v46, v36, v37
	v_cvt_pk_fp8_f32 v47, v40, v41
	v_cvt_pk_fp8_f32 v44, v30, v31 op_sel:[0,0,1]
	v_cvt_pk_fp8_f32 v45, v34, v35 op_sel:[0,0,1]
	v_cvt_pk_fp8_f32 v46, v38, v39 op_sel:[0,0,1]
	v_cvt_pk_fp8_f32 v47, v42, v43 op_sel:[0,0,1]
	s_nop 1
	v_permlane16_swap_b32 v44, v46
	v_permlane16_swap_b32 v45, v47
	s_nop 1
	global_store_dwordx4 v[20:21], v[44:47], off nt
	v_pk_fma_f32 v[28:29], v[150:151], s[16:17], v[6:7] op_sel_hi:[1,0,1]
	v_pk_fma_f32 v[30:31], v[152:153], s[16:17], v[8:9] op_sel_hi:[1,0,1]
	v_pk_fma_f32 v[32:33], v[142:143], s[16:17], v[2:3] op_sel_hi:[1,0,1]
	v_pk_fma_f32 v[34:35], v[144:145], s[16:17], v[4:5] op_sel_hi:[1,0,1]
	v_pk_fma_f32 v[36:37], v[134:135], s[16:17], v[6:7] op_sel_hi:[1,0,1]
	v_pk_fma_f32 v[38:39], v[136:137], s[16:17], v[8:9] op_sel_hi:[1,0,1]
	v_pk_fma_f32 v[40:41], v[130:131], s[16:17], v[2:3] op_sel_hi:[1,0,1]
	v_pk_fma_f32 v[42:43], v[132:133], s[16:17], v[4:5] op_sel_hi:[1,0,1]
	v_pk_mul_f32 v[28:29], v[28:29], s[18:19] op_sel_hi:[1,0]
	v_pk_mul_f32 v[30:31], v[30:31], s[18:19] op_sel_hi:[1,0]
	v_pk_mul_f32 v[32:33], v[32:33], s[18:19] op_sel_hi:[1,0]
	v_pk_mul_f32 v[34:35], v[34:35], s[18:19] op_sel_hi:[1,0]
	v_pk_mul_f32 v[36:37], v[36:37], s[18:19] op_sel_hi:[1,0]
	v_pk_mul_f32 v[38:39], v[38:39], s[18:19] op_sel_hi:[1,0]
	v_pk_mul_f32 v[40:41], v[40:41], s[18:19] op_sel_hi:[1,0]
	v_pk_mul_f32 v[42:43], v[42:43], s[18:19] op_sel_hi:[1,0]
	v_mov_b32_e32 v48, v205
	v_mov_b32_e32 v49, v205
	v_mov_b32_e32 v50, v205
	v_mov_b32_e32 v51, v205
	v_cvt_pk_fp8_f32 v48, v28, v29
	v_cvt_pk_fp8_f32 v49, v32, v33
	v_cvt_pk_fp8_f32 v50, v36, v37
	v_cvt_pk_fp8_f32 v51, v40, v41
	v_cvt_pk_fp8_f32 v48, v30, v31 op_sel:[0,0,1]
	v_cvt_pk_fp8_f32 v49, v34, v35 op_sel:[0,0,1]
	v_cvt_pk_fp8_f32 v50, v38, v39 op_sel:[0,0,1]
	v_cvt_pk_fp8_f32 v51, v42, v43 op_sel:[0,0,1]
	s_nop 1
	v_permlane16_swap_b32 v48, v50
	v_permlane16_swap_b32 v49, v51
	s_nop 1
	global_store_dwordx4 v[20:21], v[48:51], off offset:128 nt
	v_lshl_add_u64 v[18:19], v[18:19], 0, v[26:27]
	v_pk_fma_f32 v[28:29], v[126:127], s[16:17], v[14:15] op_sel_hi:[1,0,1]
	v_pk_fma_f32 v[30:31], v[128:129], s[16:17], v[16:17] op_sel_hi:[1,0,1]
	v_pk_fma_f32 v[32:33], v[122:123], s[16:17], v[10:11] op_sel_hi:[1,0,1]
	v_pk_fma_f32 v[34:35], v[124:125], s[16:17], v[12:13] op_sel_hi:[1,0,1]
	v_pk_fma_f32 v[36:37], v[114:115], s[16:17], v[14:15] op_sel_hi:[1,0,1]
	v_pk_fma_f32 v[38:39], v[116:117], s[16:17], v[16:17] op_sel_hi:[1,0,1]
	v_pk_fma_f32 v[40:41], v[106:107], s[16:17], v[10:11] op_sel_hi:[1,0,1]
	v_pk_fma_f32 v[42:43], v[108:109], s[16:17], v[12:13] op_sel_hi:[1,0,1]
	v_pk_mul_f32 v[28:29], v[28:29], s[18:19] op_sel_hi:[1,0]
	v_pk_mul_f32 v[30:31], v[30:31], s[18:19] op_sel_hi:[1,0]
	v_pk_mul_f32 v[32:33], v[32:33], s[18:19] op_sel_hi:[1,0]
	v_pk_mul_f32 v[34:35], v[34:35], s[18:19] op_sel_hi:[1,0]
	v_pk_mul_f32 v[36:37], v[36:37], s[18:19] op_sel_hi:[1,0]
	v_pk_mul_f32 v[38:39], v[38:39], s[18:19] op_sel_hi:[1,0]
	v_pk_mul_f32 v[40:41], v[40:41], s[18:19] op_sel_hi:[1,0]
	v_pk_mul_f32 v[42:43], v[42:43], s[18:19] op_sel_hi:[1,0]
	v_mov_b32_e32 v44, v205
	v_mov_b32_e32 v45, v205
	v_mov_b32_e32 v46, v205
	v_mov_b32_e32 v47, v205
	v_cvt_pk_fp8_f32 v44, v28, v29
	v_cvt_pk_fp8_f32 v45, v32, v33
	v_cvt_pk_fp8_f32 v46, v36, v37
	v_cvt_pk_fp8_f32 v47, v40, v41
	v_cvt_pk_fp8_f32 v44, v30, v31 op_sel:[0,0,1]
	v_cvt_pk_fp8_f32 v45, v34, v35 op_sel:[0,0,1]
	v_cvt_pk_fp8_f32 v46, v38, v39 op_sel:[0,0,1]
	v_cvt_pk_fp8_f32 v47, v42, v43 op_sel:[0,0,1]
	s_nop 1
	v_permlane16_swap_b32 v44, v46
	v_permlane16_swap_b32 v45, v47
	s_nop 1
	global_store_dwordx4 v[18:19], v[44:47], off nt
	v_pk_fma_f32 v[28:29], v[118:119], s[16:17], v[6:7] op_sel_hi:[1,0,1]
	v_pk_fma_f32 v[30:31], v[120:121], s[16:17], v[8:9] op_sel_hi:[1,0,1]
	v_pk_fma_f32 v[32:33], v[110:111], s[16:17], v[2:3] op_sel_hi:[1,0,1]
	v_pk_fma_f32 v[34:35], v[112:113], s[16:17], v[4:5] op_sel_hi:[1,0,1]
	v_pk_fma_f32 v[36:37], v[102:103], s[16:17], v[6:7] op_sel_hi:[1,0,1]
	v_pk_fma_f32 v[38:39], v[104:105], s[16:17], v[8:9] op_sel_hi:[1,0,1]
	v_pk_fma_f32 v[40:41], v[94:95], s[16:17], v[2:3] op_sel_hi:[1,0,1]
	v_pk_fma_f32 v[42:43], v[96:97], s[16:17], v[4:5] op_sel_hi:[1,0,1]
	v_pk_mul_f32 v[28:29], v[28:29], s[18:19] op_sel_hi:[1,0]
	v_pk_mul_f32 v[30:31], v[30:31], s[18:19] op_sel_hi:[1,0]
	v_pk_mul_f32 v[32:33], v[32:33], s[18:19] op_sel_hi:[1,0]
	v_pk_mul_f32 v[34:35], v[34:35], s[18:19] op_sel_hi:[1,0]
	v_pk_mul_f32 v[36:37], v[36:37], s[18:19] op_sel_hi:[1,0]
	v_pk_mul_f32 v[38:39], v[38:39], s[18:19] op_sel_hi:[1,0]
	v_pk_mul_f32 v[40:41], v[40:41], s[18:19] op_sel_hi:[1,0]
	v_pk_mul_f32 v[42:43], v[42:43], s[18:19] op_sel_hi:[1,0]
	v_mov_b32_e32 v48, v205
	v_mov_b32_e32 v49, v205
	v_mov_b32_e32 v50, v205
	v_mov_b32_e32 v51, v205
	v_cvt_pk_fp8_f32 v48, v28, v29
	v_cvt_pk_fp8_f32 v49, v32, v33
	v_cvt_pk_fp8_f32 v50, v36, v37
	v_cvt_pk_fp8_f32 v51, v40, v41
	v_cvt_pk_fp8_f32 v48, v30, v31 op_sel:[0,0,1]
	v_cvt_pk_fp8_f32 v49, v34, v35 op_sel:[0,0,1]
	v_cvt_pk_fp8_f32 v50, v38, v39 op_sel:[0,0,1]
	v_cvt_pk_fp8_f32 v51, v42, v43 op_sel:[0,0,1]
	s_nop 1
	v_permlane16_swap_b32 v48, v50
	v_permlane16_swap_b32 v49, v51
	s_nop 1
	global_store_dwordx4 v[18:19], v[48:51], off offset:128 nt
	v_lshl_add_u64 v[20:21], v[18:19], 0, v[24:25]
	v_pk_fma_f32 v[28:29], v[98:99], s[16:17], v[14:15] op_sel_hi:[1,0,1]
	v_pk_fma_f32 v[30:31], v[100:101], s[16:17], v[16:17] op_sel_hi:[1,0,1]
	v_pk_fma_f32 v[32:33], v[90:91], s[16:17], v[10:11] op_sel_hi:[1,0,1]
	v_pk_fma_f32 v[34:35], v[92:93], s[16:17], v[12:13] op_sel_hi:[1,0,1]
	v_pk_fma_f32 v[36:37], v[82:83], s[16:17], v[14:15] op_sel_hi:[1,0,1]
	v_pk_fma_f32 v[38:39], v[84:85], s[16:17], v[16:17] op_sel_hi:[1,0,1]
	v_pk_fma_f32 v[40:41], v[74:75], s[16:17], v[10:11] op_sel_hi:[1,0,1]
	v_pk_fma_f32 v[42:43], v[76:77], s[16:17], v[12:13] op_sel_hi:[1,0,1]
	v_pk_mul_f32 v[28:29], v[28:29], s[18:19] op_sel_hi:[1,0]
	v_pk_mul_f32 v[30:31], v[30:31], s[18:19] op_sel_hi:[1,0]
	v_pk_mul_f32 v[32:33], v[32:33], s[18:19] op_sel_hi:[1,0]
	v_pk_mul_f32 v[34:35], v[34:35], s[18:19] op_sel_hi:[1,0]
	v_pk_mul_f32 v[36:37], v[36:37], s[18:19] op_sel_hi:[1,0]
	v_pk_mul_f32 v[38:39], v[38:39], s[18:19] op_sel_hi:[1,0]
	v_pk_mul_f32 v[40:41], v[40:41], s[18:19] op_sel_hi:[1,0]
	v_pk_mul_f32 v[42:43], v[42:43], s[18:19] op_sel_hi:[1,0]
	v_mov_b32_e32 v44, v205
	v_mov_b32_e32 v45, v205
	v_mov_b32_e32 v46, v205
	v_mov_b32_e32 v47, v205
	v_cvt_pk_fp8_f32 v44, v28, v29
	v_cvt_pk_fp8_f32 v45, v32, v33
	v_cvt_pk_fp8_f32 v46, v36, v37
	v_cvt_pk_fp8_f32 v47, v40, v41
	v_cvt_pk_fp8_f32 v44, v30, v31 op_sel:[0,0,1]
	v_cvt_pk_fp8_f32 v45, v34, v35 op_sel:[0,0,1]
	v_cvt_pk_fp8_f32 v46, v38, v39 op_sel:[0,0,1]
	v_cvt_pk_fp8_f32 v47, v42, v43 op_sel:[0,0,1]
	s_nop 1
	v_permlane16_swap_b32 v44, v46
	v_permlane16_swap_b32 v45, v47
	s_nop 1
	global_store_dwordx4 v[20:21], v[44:47], off nt
	v_pk_fma_f32 v[28:29], v[86:87], s[16:17], v[6:7] op_sel_hi:[1,0,1]
	v_pk_fma_f32 v[30:31], v[88:89], s[16:17], v[8:9] op_sel_hi:[1,0,1]
	v_pk_fma_f32 v[32:33], v[78:79], s[16:17], v[2:3] op_sel_hi:[1,0,1]
	v_pk_fma_f32 v[34:35], v[80:81], s[16:17], v[4:5] op_sel_hi:[1,0,1]
	v_pk_fma_f32 v[36:37], v[70:71], s[16:17], v[6:7] op_sel_hi:[1,0,1]
	v_pk_fma_f32 v[38:39], v[72:73], s[16:17], v[8:9] op_sel_hi:[1,0,1]
	v_pk_fma_f32 v[40:41], v[66:67], s[16:17], v[2:3] op_sel_hi:[1,0,1]
	v_pk_fma_f32 v[42:43], v[68:69], s[16:17], v[4:5] op_sel_hi:[1,0,1]
	v_pk_mul_f32 v[28:29], v[28:29], s[18:19] op_sel_hi:[1,0]
	v_pk_mul_f32 v[30:31], v[30:31], s[18:19] op_sel_hi:[1,0]
	v_pk_mul_f32 v[32:33], v[32:33], s[18:19] op_sel_hi:[1,0]
	v_pk_mul_f32 v[34:35], v[34:35], s[18:19] op_sel_hi:[1,0]
	v_pk_mul_f32 v[36:37], v[36:37], s[18:19] op_sel_hi:[1,0]
	v_pk_mul_f32 v[38:39], v[38:39], s[18:19] op_sel_hi:[1,0]
	v_pk_mul_f32 v[40:41], v[40:41], s[18:19] op_sel_hi:[1,0]
	v_pk_mul_f32 v[42:43], v[42:43], s[18:19] op_sel_hi:[1,0]
	v_mov_b32_e32 v48, v205
	v_mov_b32_e32 v49, v205
	v_mov_b32_e32 v50, v205
	v_mov_b32_e32 v51, v205
	v_cvt_pk_fp8_f32 v48, v28, v29
	v_cvt_pk_fp8_f32 v49, v32, v33
	v_cvt_pk_fp8_f32 v50, v36, v37
	v_cvt_pk_fp8_f32 v51, v40, v41
	v_cvt_pk_fp8_f32 v48, v30, v31 op_sel:[0,0,1]
	v_cvt_pk_fp8_f32 v49, v34, v35 op_sel:[0,0,1]
	v_cvt_pk_fp8_f32 v50, v38, v39 op_sel:[0,0,1]
	v_cvt_pk_fp8_f32 v51, v42, v43 op_sel:[0,0,1]
	s_nop 1
	v_permlane16_swap_b32 v48, v50
	v_permlane16_swap_b32 v49, v51
	s_nop 1
	global_store_dwordx4 v[20:21], v[48:51], off offset:128 nt
	s_andn2_b64 vcc, exec, s[8:9]
	s_mov_b64 s[8:9], -1
	s_cbranch_vccnz .LBB0_1350
	s_andn2_b64 vcc, exec, s[6:7]
	s_cbranch_vccnz .LBB0_1349
	s_barrier
	s_branch .LBB0_1349
